# memory cross-attention epilogue: e4m3 output tile staged per wave through the dead LDS image and written as 8 16-byte row pieces per lane instead of 128 single-byte global stores
# baseline (speedup 1.0000x reference)
; #define LAS __attribute__((address_space(3)))
; __device__ __forceinline__ void xattn_unit(Frame& F, const bf16* XQ, unsigned char* XO  , const bf16* MEMK, const bf16* MEMVT, int pm, int h) {
;     ...
;     f32x16 o[8];
; #pragma unroll
;     for (int db = 0; db < 8; ++db) { o[db] = (f32x16){};
;         const LAS unsigned char* vr = F.lds + RING_OFF + (db * 32 + r32) * XA_ROWB + hi * 8;
; #pragma unroll
;         for (int ks = 0; ks < 16; ++ks) { const pg8::u32x2 lo = *(const LAS pg8::u32x2*)(vr + ks * 32), hh = *(const LAS pg8::u32x2*)(vr + ks * 32 + 16);
;             const v4u vv = (v4u){lo.x, lo.y, hh.x, hh.y};
;             o[db] = __builtin_amdgcn_mfma_f32_32x32x16_bf16(__builtin_bit_cast(bf16x8, pk[ks >> 1][ks & 1]), __builtin_bit_cast(bf16x8, vv), o[db], 0, 0, 0); if ((ks & 3) == 3) asm volatile("" ::: "memory"); } }
.LBB0_1506:
	s_or_b64 exec, exec, s[4:5]
	s_waitcnt lgkmcnt(0)
	s_barrier
	ds_read2_b64 v[4:7], v230 offset1:2
	ds_read2_b64 v[8:11], v230 offset0:4 offset1:6
	s_waitcnt lgkmcnt(1)
	v_mfma_f32_32x32x16_bf16 v[116:131], v[152:155], v[4:7], 0
	ds_read2_b64 v[4:7], v230 offset0:8 offset1:10
	v_add_u32_e32 v2, 0x4000, v230
	s_add_i32 s19, s19, 1
	s_waitcnt lgkmcnt(1)
	v_mfma_f32_32x32x16_bf16 v[116:131], v[156:159], v[8:11], v[116:131]
	s_waitcnt lgkmcnt(0)
	v_mfma_f32_32x32x16_bf16 v[116:131], v[136:139], v[4:7], v[116:131]
	ds_read2_b64 v[4:7], v230 offset0:12 offset1:14
	s_waitcnt lgkmcnt(0)
	v_mfma_f32_32x32x16_bf16 v[116:131], v[132:135], v[4:7], v[116:131]
	ds_read2_b64 v[4:7], v230 offset0:16 offset1:18
	ds_read2_b64 v[8:11], v230 offset0:20 offset1:22
	s_waitcnt lgkmcnt(1)
	v_mfma_f32_32x32x16_bf16 v[116:131], v[140:143], v[4:7], v[116:131]
	ds_read2_b64 v[4:7], v230 offset0:24 offset1:26
	s_waitcnt lgkmcnt(1)
	v_mfma_f32_32x32x16_bf16 v[116:131], v[144:147], v[8:11], v[116:131]
	s_waitcnt lgkmcnt(0)
	v_mfma_f32_32x32x16_bf16 v[116:131], v[160:163], v[4:7], v[116:131]
	ds_read2_b64 v[4:7], v230 offset0:28 offset1:30
	s_waitcnt lgkmcnt(0)
	v_mfma_f32_32x32x16_bf16 v[116:131], v[148:151], v[4:7], v[116:131]
	ds_read2_b64 v[4:7], v230 offset0:32 offset1:34
	ds_read2_b64 v[8:11], v230 offset0:36 offset1:38
	s_waitcnt lgkmcnt(1)
	v_mfma_f32_32x32x16_bf16 v[116:131], v[164:167], v[4:7], v[116:131]
	ds_read2_b64 v[4:7], v230 offset0:40 offset1:42
	s_waitcnt lgkmcnt(1)
	v_mfma_f32_32x32x16_bf16 v[116:131], v[168:171], v[8:11], v[116:131]
	s_waitcnt lgkmcnt(0)
	v_mfma_f32_32x32x16_bf16 v[116:131], v[176:179], v[4:7], v[116:131]
	ds_read2_b64 v[4:7], v230 offset0:44 offset1:46
	s_waitcnt lgkmcnt(0)
	v_mfma_f32_32x32x16_bf16 v[116:131], v[172:175], v[4:7], v[116:131]
	ds_read2_b64 v[4:7], v230 offset0:48 offset1:50
	ds_read2_b64 v[8:11], v230 offset0:52 offset1:54
	s_waitcnt lgkmcnt(1)
	v_mfma_f32_32x32x16_bf16 v[116:131], v[180:183], v[4:7], v[116:131]
	ds_read2_b64 v[4:7], v230 offset0:56 offset1:58
	s_waitcnt lgkmcnt(1)
	v_mfma_f32_32x32x16_bf16 v[116:131], v[184:187], v[8:11], v[116:131]
	s_waitcnt lgkmcnt(0)
	v_mfma_f32_32x32x16_bf16 v[116:131], v[192:195], v[4:7], v[116:131]
	ds_read2_b64 v[4:7], v230 offset0:60 offset1:62
	s_waitcnt lgkmcnt(0)
	v_mfma_f32_32x32x16_bf16 v[116:131], v[188:191], v[4:7], v[116:131]
	ds_read2_b64 v[4:7], v2 offset0:64 offset1:66
	ds_read2_b64 v[8:11], v2 offset0:68 offset1:70
	s_waitcnt lgkmcnt(1)
	v_mfma_f32_32x32x16_bf16 v[100:115], v[152:155], v[4:7], 0
	ds_read2_b64 v[4:7], v2 offset0:72 offset1:74
	s_waitcnt lgkmcnt(1)
	v_mfma_f32_32x32x16_bf16 v[100:115], v[156:159], v[8:11], v[100:115]
	s_waitcnt lgkmcnt(0)
	v_mfma_f32_32x32x16_bf16 v[100:115], v[136:139], v[4:7], v[100:115]
	ds_read2_b64 v[4:7], v2 offset0:76 offset1:78
	s_waitcnt lgkmcnt(0)
	v_mfma_f32_32x32x16_bf16 v[100:115], v[132:135], v[4:7], v[100:115]
	ds_read2_b64 v[4:7], v2 offset0:80 offset1:82
	ds_read2_b64 v[8:11], v2 offset0:84 offset1:86
	s_waitcnt lgkmcnt(1)
	v_mfma_f32_32x32x16_bf16 v[100:115], v[140:143], v[4:7], v[100:115]
	ds_read2_b64 v[4:7], v2 offset0:88 offset1:90
	s_waitcnt lgkmcnt(1)
	v_mfma_f32_32x32x16_bf16 v[100:115], v[144:147], v[8:11], v[100:115]
	s_waitcnt lgkmcnt(0)
	v_mfma_f32_32x32x16_bf16 v[100:115], v[160:163], v[4:7], v[100:115]
	ds_read2_b64 v[4:7], v2 offset0:92 offset1:94
	s_waitcnt lgkmcnt(0)
	v_mfma_f32_32x32x16_bf16 v[100:115], v[148:151], v[4:7], v[100:115]
	ds_read2_b64 v[4:7], v2 offset0:96 offset1:98
	ds_read2_b64 v[8:11], v2 offset0:100 offset1:102
	s_waitcnt lgkmcnt(1)
	v_mfma_f32_32x32x16_bf16 v[100:115], v[164:167], v[4:7], v[100:115]
	ds_read2_b64 v[4:7], v2 offset0:104 offset1:106
	s_waitcnt lgkmcnt(1)
	v_mfma_f32_32x32x16_bf16 v[100:115], v[168:171], v[8:11], v[100:115]
	s_waitcnt lgkmcnt(0)
	v_mfma_f32_32x32x16_bf16 v[100:115], v[176:179], v[4:7], v[100:115]
	ds_read2_b64 v[4:7], v2 offset0:108 offset1:110
	s_waitcnt lgkmcnt(0)
	v_mfma_f32_32x32x16_bf16 v[100:115], v[172:175], v[4:7], v[100:115]
	ds_read2_b64 v[4:7], v2 offset0:112 offset1:114
	ds_read2_b64 v[8:11], v2 offset0:116 offset1:118
	s_waitcnt lgkmcnt(1)
	v_mfma_f32_32x32x16_bf16 v[100:115], v[180:183], v[4:7], v[100:115]
	ds_read2_b64 v[4:7], v2 offset0:120 offset1:122
	s_waitcnt lgkmcnt(1)
	v_mfma_f32_32x32x16_bf16 v[100:115], v[184:187], v[8:11], v[100:115]
	s_waitcnt lgkmcnt(0)
	v_mfma_f32_32x32x16_bf16 v[100:115], v[192:195], v[4:7], v[100:115]
	ds_read2_b64 v[4:7], v2 offset0:124 offset1:126
	v_add_u32_e32 v2, 0x8000, v230
	s_waitcnt lgkmcnt(0)
	v_mfma_f32_32x32x16_bf16 v[100:115], v[188:191], v[4:7], v[100:115]
	ds_read2_b64 v[4:7], v2 offset0:128 offset1:130
	ds_read2_b64 v[8:11], v2 offset0:132 offset1:134
	s_waitcnt lgkmcnt(1)
	v_mfma_f32_32x32x16_bf16 v[84:99], v[152:155], v[4:7], 0
	ds_read2_b64 v[4:7], v2 offset0:136 offset1:138
	s_waitcnt lgkmcnt(1)
	v_mfma_f32_32x32x16_bf16 v[84:99], v[156:159], v[8:11], v[84:99]
	s_waitcnt lgkmcnt(0)
	v_mfma_f32_32x32x16_bf16 v[84:99], v[136:139], v[4:7], v[84:99]
	ds_read2_b64 v[4:7], v2 offset0:140 offset1:142
	s_waitcnt lgkmcnt(0)
	v_mfma_f32_32x32x16_bf16 v[84:99], v[132:135], v[4:7], v[84:99]
	ds_read2_b64 v[4:7], v2 offset0:144 offset1:146
	ds_read2_b64 v[8:11], v2 offset0:148 offset1:150
	s_waitcnt lgkmcnt(1)
	v_mfma_f32_32x32x16_bf16 v[84:99], v[140:143], v[4:7], v[84:99]
	ds_read2_b64 v[4:7], v2 offset0:152 offset1:154
	s_waitcnt lgkmcnt(1)
	v_mfma_f32_32x32x16_bf16 v[84:99], v[144:147], v[8:11], v[84:99]
	s_waitcnt lgkmcnt(0)
	v_mfma_f32_32x32x16_bf16 v[84:99], v[160:163], v[4:7], v[84:99]
	ds_read2_b64 v[4:7], v2 offset0:156 offset1:158
	s_waitcnt lgkmcnt(0)
; #define LAS __attribute__((address_space(3)))
; __device__ __forceinline__ void xattn_unit(Frame& F, const bf16* XQ, unsigned char* XO  , const bf16* MEMK, const bf16* MEMVT, int pm, int h) {
;     ...
;     f32x16 o[8];
; #pragma unroll
;     for (int db = 0; db < 8; ++db) { o[db] = (f32x16){};
;         const LAS unsigned char* vr = F.lds + RING_OFF + (db * 32 + r32) * XA_ROWB + hi * 8;
; #pragma unroll
;         for (int ks = 0; ks < 16; ++ks) { const pg8::u32x2 lo = *(const LAS pg8::u32x2*)(vr + ks * 32), hh = *(const LAS pg8::u32x2*)(vr + ks * 32 + 16);
;             const v4u vv = (v4u){lo.x, lo.y, hh.x, hh.y};
;             o[db] = __builtin_amdgcn_mfma_f32_32x32x16_bf16(__builtin_bit_cast(bf16x8, pk[ks >> 1][ks & 1]), __builtin_bit_cast(bf16x8, vv), o[db], 0, 0, 0); if ((ks & 3) == 3) asm volatile("" ::: "memory"); } }
	v_mfma_f32_32x32x16_bf16 v[84:99], v[148:151], v[4:7], v[84:99]
	ds_read2_b64 v[4:7], v2 offset0:160 offset1:162
	ds_read2_b64 v[8:11], v2 offset0:164 offset1:166
	s_waitcnt lgkmcnt(1)
	v_mfma_f32_32x32x16_bf16 v[84:99], v[164:167], v[4:7], v[84:99]
	ds_read2_b64 v[4:7], v2 offset0:168 offset1:170
	s_waitcnt lgkmcnt(1)
	v_mfma_f32_32x32x16_bf16 v[84:99], v[168:171], v[8:11], v[84:99]
	s_waitcnt lgkmcnt(0)
	v_mfma_f32_32x32x16_bf16 v[84:99], v[176:179], v[4:7], v[84:99]
	ds_read2_b64 v[4:7], v2 offset0:172 offset1:174
	s_waitcnt lgkmcnt(0)
	v_mfma_f32_32x32x16_bf16 v[84:99], v[172:175], v[4:7], v[84:99]
	ds_read2_b64 v[4:7], v2 offset0:176 offset1:178
	ds_read2_b64 v[8:11], v2 offset0:180 offset1:182
	s_waitcnt lgkmcnt(1)
	v_mfma_f32_32x32x16_bf16 v[84:99], v[180:183], v[4:7], v[84:99]
	ds_read2_b64 v[4:7], v2 offset0:184 offset1:186
	s_waitcnt lgkmcnt(1)
	v_mfma_f32_32x32x16_bf16 v[84:99], v[184:187], v[8:11], v[84:99]
	s_waitcnt lgkmcnt(0)
	v_mfma_f32_32x32x16_bf16 v[84:99], v[192:195], v[4:7], v[84:99]
	ds_read2_b64 v[4:7], v2 offset0:188 offset1:190
	v_add_u32_e32 v2, 0xc000, v230
	s_waitcnt lgkmcnt(0)
	v_mfma_f32_32x32x16_bf16 v[84:99], v[188:191], v[4:7], v[84:99]
	ds_read2_b64 v[4:7], v2 offset0:192 offset1:194
	ds_read2_b64 v[8:11], v2 offset0:196 offset1:198
	s_waitcnt lgkmcnt(1)
	v_mfma_f32_32x32x16_bf16 v[68:83], v[152:155], v[4:7], 0
	ds_read2_b64 v[4:7], v2 offset0:200 offset1:202
	s_waitcnt lgkmcnt(1)
	v_mfma_f32_32x32x16_bf16 v[68:83], v[156:159], v[8:11], v[68:83]
	s_waitcnt lgkmcnt(0)
	v_mfma_f32_32x32x16_bf16 v[68:83], v[136:139], v[4:7], v[68:83]
	ds_read2_b64 v[4:7], v2 offset0:204 offset1:206
	s_waitcnt lgkmcnt(0)
	v_mfma_f32_32x32x16_bf16 v[68:83], v[132:135], v[4:7], v[68:83]
	ds_read2_b64 v[4:7], v2 offset0:208 offset1:210
	ds_read2_b64 v[8:11], v2 offset0:212 offset1:214
	s_waitcnt lgkmcnt(1)
	v_mfma_f32_32x32x16_bf16 v[68:83], v[140:143], v[4:7], v[68:83]
	ds_read2_b64 v[4:7], v2 offset0:216 offset1:218
	s_waitcnt lgkmcnt(1)
	v_mfma_f32_32x32x16_bf16 v[68:83], v[144:147], v[8:11], v[68:83]
	s_waitcnt lgkmcnt(0)
	v_mfma_f32_32x32x16_bf16 v[68:83], v[160:163], v[4:7], v[68:83]
	ds_read2_b64 v[4:7], v2 offset0:220 offset1:222
	s_waitcnt lgkmcnt(0)
	v_mfma_f32_32x32x16_bf16 v[68:83], v[148:151], v[4:7], v[68:83]
	ds_read2_b64 v[4:7], v2 offset0:224 offset1:226
	ds_read2_b64 v[8:11], v2 offset0:228 offset1:230
	s_waitcnt lgkmcnt(1)
	v_mfma_f32_32x32x16_bf16 v[68:83], v[164:167], v[4:7], v[68:83]
	ds_read2_b64 v[4:7], v2 offset0:232 offset1:234
	s_waitcnt lgkmcnt(1)
	v_mfma_f32_32x32x16_bf16 v[68:83], v[168:171], v[8:11], v[68:83]
	s_waitcnt lgkmcnt(0)
	v_mfma_f32_32x32x16_bf16 v[68:83], v[176:179], v[4:7], v[68:83]
	ds_read2_b64 v[4:7], v2 offset0:236 offset1:238
	s_waitcnt lgkmcnt(0)
	v_mfma_f32_32x32x16_bf16 v[68:83], v[172:175], v[4:7], v[68:83]
	ds_read2_b64 v[4:7], v2 offset0:240 offset1:242
	ds_read2_b64 v[8:11], v2 offset0:244 offset1:246
	s_waitcnt lgkmcnt(1)
	v_mfma_f32_32x32x16_bf16 v[68:83], v[180:183], v[4:7], v[68:83]
	ds_read2_b64 v[4:7], v2 offset0:248 offset1:250
	s_waitcnt lgkmcnt(1)
	v_mfma_f32_32x32x16_bf16 v[68:83], v[184:187], v[8:11], v[68:83]
	s_waitcnt lgkmcnt(0)
	v_mfma_f32_32x32x16_bf16 v[68:83], v[192:195], v[4:7], v[68:83]
	ds_read2_b64 v[4:7], v2 offset0:252 offset1:254
	v_add_u32_e32 v2, v224, v214
	s_waitcnt lgkmcnt(0)
	v_mfma_f32_32x32x16_bf16 v[68:83], v[188:191], v[4:7], v[68:83]
	ds_read2_b64 v[4:7], v2 offset1:2
	ds_read2_b64 v[8:11], v2 offset0:4 offset1:6
	s_waitcnt lgkmcnt(1)
	v_mfma_f32_32x32x16_bf16 v[52:67], v[152:155], v[4:7], 0
	ds_read2_b64 v[4:7], v2 offset0:8 offset1:10
	s_waitcnt lgkmcnt(1)
	v_mfma_f32_32x32x16_bf16 v[52:67], v[156:159], v[8:11], v[52:67]
	s_waitcnt lgkmcnt(0)
	v_mfma_f32_32x32x16_bf16 v[52:67], v[136:139], v[4:7], v[52:67]
	ds_read2_b64 v[4:7], v2 offset0:12 offset1:14
	s_waitcnt lgkmcnt(0)
	v_mfma_f32_32x32x16_bf16 v[52:67], v[132:135], v[4:7], v[52:67]
	ds_read2_b64 v[4:7], v2 offset0:16 offset1:18
	ds_read2_b64 v[8:11], v2 offset0:20 offset1:22
	s_waitcnt lgkmcnt(1)
	v_mfma_f32_32x32x16_bf16 v[52:67], v[140:143], v[4:7], v[52:67]
	ds_read2_b64 v[4:7], v2 offset0:24 offset1:26
	s_waitcnt lgkmcnt(1)
	v_mfma_f32_32x32x16_bf16 v[52:67], v[144:147], v[8:11], v[52:67]
	s_waitcnt lgkmcnt(0)
	v_mfma_f32_32x32x16_bf16 v[52:67], v[160:163], v[4:7], v[52:67]
	ds_read2_b64 v[4:7], v2 offset0:28 offset1:30
	s_waitcnt lgkmcnt(0)
	v_mfma_f32_32x32x16_bf16 v[52:67], v[148:151], v[4:7], v[52:67]
	ds_read2_b64 v[4:7], v2 offset0:32 offset1:34
	ds_read2_b64 v[8:11], v2 offset0:36 offset1:38
	s_waitcnt lgkmcnt(1)
	v_mfma_f32_32x32x16_bf16 v[52:67], v[164:167], v[4:7], v[52:67]
	ds_read2_b64 v[4:7], v2 offset0:40 offset1:42
	s_waitcnt lgkmcnt(1)
	v_mfma_f32_32x32x16_bf16 v[52:67], v[168:171], v[8:11], v[52:67]
	s_waitcnt lgkmcnt(0)
	v_mfma_f32_32x32x16_bf16 v[52:67], v[176:179], v[4:7], v[52:67]
	ds_read2_b64 v[4:7], v2 offset0:44 offset1:46
	s_waitcnt lgkmcnt(0)
	v_mfma_f32_32x32x16_bf16 v[52:67], v[172:175], v[4:7], v[52:67]
	ds_read2_b64 v[4:7], v2 offset0:48 offset1:50
	ds_read2_b64 v[8:11], v2 offset0:52 offset1:54
	s_waitcnt lgkmcnt(1)
	v_mfma_f32_32x32x16_bf16 v[52:67], v[180:183], v[4:7], v[52:67]
	ds_read2_b64 v[4:7], v2 offset0:56 offset1:58
	s_waitcnt lgkmcnt(1)
	v_mfma_f32_32x32x16_bf16 v[52:67], v[184:187], v[8:11], v[52:67]
	s_waitcnt lgkmcnt(0)
	v_mfma_f32_32x32x16_bf16 v[52:67], v[192:195], v[4:7], v[52:67]
	ds_read2_b64 v[4:7], v2 offset0:60 offset1:62
	v_add_u32_e32 v2, v225, v214
	s_waitcnt lgkmcnt(0)
	v_mfma_f32_32x32x16_bf16 v[52:67], v[188:191], v[4:7], v[52:67]
	ds_read2_b64 v[4:7], v2 offset1:2
	ds_read2_b64 v[20:23], v2 offset0:4 offset1:6
	s_waitcnt lgkmcnt(1)
; #define LAS __attribute__((address_space(3)))
; __device__ __forceinline__ int crow(int r, int hi) { return (r & 3) + 8 * (r >> 2) + 4 * hi; }
; __device__ __forceinline__ int crow(int r,int hi){return (r&3)+8*(r>>2)+4*hi;}
; __device__ __forceinline__ void xattn_unit(Frame& F, const bf16* XQ, unsigned char* XO  , const bf16* MEMK, const bf16* MEMVT, int pm, int h) {
;     ...
;     f32x16 o[8];
; #pragma unroll
;     for (int db = 0; db < 8; ++db) { o[db] = (f32x16){};
;         const LAS unsigned char* vr = F.lds + RING_OFF + (db * 32 + r32) * XA_ROWB + hi * 8;
; #pragma unroll
;         for (int ks = 0; ks < 16; ++ks) { const pg8::u32x2 lo = *(const LAS pg8::u32x2*)(vr + ks * 32), hh = *(const LAS pg8::u32x2*)(vr + ks * 32 + 16);
;             const v4u vv = (v4u){lo.x, lo.y, hh.x, hh.y};
;             o[db] = __builtin_amdgcn_mfma_f32_32x32x16_bf16(__builtin_bit_cast(bf16x8, pk[ks >> 1][ks & 1]), __builtin_bit_cast(bf16x8, vv), o[db], 0, 0, 0); if ((ks & 3) == 3) asm volatile("" ::: "memory"); } }
;     float rl[16];
; #pragma unroll
;     for (int r = 0; r < 16; ++r) rl[r] = 1.0f / wsf[crow(r, hi)];
	v_mfma_f32_32x32x16_bf16 v[4:19], v[152:155], v[4:7], 0
	s_waitcnt lgkmcnt(0)
	v_mfma_f32_32x32x16_bf16 v[4:19], v[156:159], v[20:23], v[4:19]
	ds_read2_b64 v[20:23], v2 offset0:8 offset1:10
	s_waitcnt lgkmcnt(0)
	v_mfma_f32_32x32x16_bf16 v[4:19], v[136:139], v[20:23], v[4:19]
	ds_read2_b64 v[20:23], v2 offset0:12 offset1:14
	s_waitcnt lgkmcnt(0)
	v_mfma_f32_32x32x16_bf16 v[4:19], v[132:135], v[20:23], v[4:19]
	ds_read2_b64 v[20:23], v2 offset0:16 offset1:18
	ds_read2_b64 v[24:27], v2 offset0:20 offset1:22
	s_waitcnt lgkmcnt(1)
	v_mfma_f32_32x32x16_bf16 v[4:19], v[140:143], v[20:23], v[4:19]
	ds_read2_b64 v[20:23], v2 offset0:24 offset1:26
	s_waitcnt lgkmcnt(1)
	v_mfma_f32_32x32x16_bf16 v[4:19], v[144:147], v[24:27], v[4:19]
	s_waitcnt lgkmcnt(0)
	v_mfma_f32_32x32x16_bf16 v[4:19], v[160:163], v[20:23], v[4:19]
	ds_read2_b64 v[20:23], v2 offset0:28 offset1:30
	s_waitcnt lgkmcnt(0)
	v_mfma_f32_32x32x16_bf16 v[4:19], v[148:151], v[20:23], v[4:19]
	ds_read2_b64 v[20:23], v2 offset0:32 offset1:34
	ds_read2_b64 v[24:27], v2 offset0:36 offset1:38
	s_waitcnt lgkmcnt(1)
	v_mfma_f32_32x32x16_bf16 v[4:19], v[164:167], v[20:23], v[4:19]
	ds_read2_b64 v[20:23], v2 offset0:40 offset1:42
	s_waitcnt lgkmcnt(1)
	v_mfma_f32_32x32x16_bf16 v[4:19], v[168:171], v[24:27], v[4:19]
	s_waitcnt lgkmcnt(0)
	v_mfma_f32_32x32x16_bf16 v[4:19], v[176:179], v[20:23], v[4:19]
	ds_read2_b64 v[20:23], v2 offset0:44 offset1:46
	s_waitcnt lgkmcnt(0)
	v_mfma_f32_32x32x16_bf16 v[4:19], v[172:175], v[20:23], v[4:19]
	ds_read2_b64 v[20:23], v2 offset0:48 offset1:50
	ds_read2_b64 v[24:27], v2 offset0:52 offset1:54
	s_waitcnt lgkmcnt(1)
	v_mfma_f32_32x32x16_bf16 v[4:19], v[180:183], v[20:23], v[4:19]
	ds_read2_b64 v[20:23], v2 offset0:56 offset1:58
	s_waitcnt lgkmcnt(1)
	v_mfma_f32_32x32x16_bf16 v[4:19], v[184:187], v[24:27], v[4:19]
	s_waitcnt lgkmcnt(0)
	v_mfma_f32_32x32x16_bf16 v[4:19], v[192:195], v[20:23], v[4:19]
	ds_read2_b64 v[20:23], v2 offset0:60 offset1:62
	v_add_u32_e32 v2, v226, v214
	s_waitcnt lgkmcnt(0)
	v_mfma_f32_32x32x16_bf16 v[4:19], v[188:191], v[20:23], v[4:19]
	ds_read2_b64 v[20:23], v2 offset1:2
	ds_read2_b64 v[36:39], v2 offset0:4 offset1:6
	s_waitcnt lgkmcnt(1)
	v_mfma_f32_32x32x16_bf16 v[20:35], v[152:155], v[20:23], 0
	s_waitcnt lgkmcnt(0)
	v_mfma_f32_32x32x16_bf16 v[20:35], v[156:159], v[36:39], v[20:35]
	ds_read2_b64 v[36:39], v2 offset0:8 offset1:10
	s_waitcnt lgkmcnt(0)
	v_mfma_f32_32x32x16_bf16 v[20:35], v[136:139], v[36:39], v[20:35]
	ds_read2_b64 v[36:39], v2 offset0:12 offset1:14
	s_waitcnt lgkmcnt(0)
	v_mfma_f32_32x32x16_bf16 v[20:35], v[132:135], v[36:39], v[20:35]
	ds_read2_b64 v[36:39], v2 offset0:16 offset1:18
	ds_read2_b64 v[40:43], v2 offset0:20 offset1:22
	s_waitcnt lgkmcnt(1)
	v_mfma_f32_32x32x16_bf16 v[20:35], v[140:143], v[36:39], v[20:35]
	ds_read2_b64 v[36:39], v2 offset0:24 offset1:26
	s_waitcnt lgkmcnt(1)
	v_mfma_f32_32x32x16_bf16 v[20:35], v[144:147], v[40:43], v[20:35]
	s_waitcnt lgkmcnt(0)
	v_mfma_f32_32x32x16_bf16 v[20:35], v[160:163], v[36:39], v[20:35]
	ds_read2_b64 v[36:39], v2 offset0:28 offset1:30
	s_waitcnt lgkmcnt(0)
	v_mfma_f32_32x32x16_bf16 v[20:35], v[148:151], v[36:39], v[20:35]
	ds_read2_b64 v[36:39], v2 offset0:32 offset1:34
	ds_read2_b64 v[40:43], v2 offset0:36 offset1:38
	s_waitcnt lgkmcnt(1)
	v_mfma_f32_32x32x16_bf16 v[20:35], v[164:167], v[36:39], v[20:35]
	ds_read2_b64 v[36:39], v2 offset0:40 offset1:42
	s_waitcnt lgkmcnt(1)
	v_mfma_f32_32x32x16_bf16 v[20:35], v[168:171], v[40:43], v[20:35]
	s_waitcnt lgkmcnt(0)
	v_mfma_f32_32x32x16_bf16 v[20:35], v[176:179], v[36:39], v[20:35]
	ds_read2_b64 v[36:39], v2 offset0:44 offset1:46
	s_waitcnt lgkmcnt(0)
	v_mfma_f32_32x32x16_bf16 v[20:35], v[172:175], v[36:39], v[20:35]
	ds_read2_b64 v[36:39], v2 offset0:48 offset1:50
	ds_read2_b64 v[40:43], v2 offset0:52 offset1:54
	s_waitcnt lgkmcnt(1)
	v_mfma_f32_32x32x16_bf16 v[20:35], v[180:183], v[36:39], v[20:35]
	ds_read2_b64 v[36:39], v2 offset0:56 offset1:58
	s_waitcnt lgkmcnt(1)
	v_mfma_f32_32x32x16_bf16 v[20:35], v[184:187], v[40:43], v[20:35]
	s_waitcnt lgkmcnt(0)
	v_mfma_f32_32x32x16_bf16 v[20:35], v[192:195], v[36:39], v[20:35]
	ds_read2_b64 v[36:39], v2 offset0:60 offset1:62
	v_add_u32_e32 v2, v228, v214
	s_waitcnt lgkmcnt(0)
	v_mfma_f32_32x32x16_bf16 v[20:35], v[188:191], v[36:39], v[20:35]
	ds_read2_b64 v[36:39], v2 offset1:2
	ds_read2_b64 v[232:235], v2 offset0:4 offset1:6
	s_waitcnt lgkmcnt(1)
	v_mfma_f32_32x32x16_bf16 v[36:51], v[152:155], v[36:39], 0
	ds_read2_b64 v[152:155], v2 offset0:8 offset1:10
	s_waitcnt lgkmcnt(1)
	v_mfma_f32_32x32x16_bf16 v[36:51], v[156:159], v[232:235], v[36:51]
	s_waitcnt lgkmcnt(0)
	v_mfma_f32_32x32x16_bf16 v[36:51], v[136:139], v[152:155], v[36:51]
	ds_read2_b64 v[136:139], v2 offset0:12 offset1:14
	s_waitcnt lgkmcnt(0)
	v_mfma_f32_32x32x16_bf16 v[36:51], v[132:135], v[136:139], v[36:51]
	ds_read2_b64 v[132:135], v2 offset0:16 offset1:18
	ds_read2_b64 v[136:139], v2 offset0:20 offset1:22
	s_waitcnt lgkmcnt(1)
	v_mfma_f32_32x32x16_bf16 v[36:51], v[140:143], v[132:135], v[36:51]
	ds_read2_b64 v[132:135], v2 offset0:24 offset1:26
	v_add_u32_e32 v140, s18, v222
	s_waitcnt lgkmcnt(1)
	v_mfma_f32_32x32x16_bf16 v[36:51], v[144:147], v[136:139], v[36:51]
	v_mov_b32_e32 v146, v3
	s_waitcnt lgkmcnt(0)
	v_mfma_f32_32x32x16_bf16 v[36:51], v[160:163], v[132:135], v[36:51]
	ds_read2_b64 v[132:135], v2 offset0:28 offset1:30
	s_waitcnt lgkmcnt(0)
	v_mfma_f32_32x32x16_bf16 v[36:51], v[148:151], v[132:135], v[36:51]
	ds_read2_b64 v[132:135], v2 offset0:32 offset1:34
	ds_read2_b64 v[136:139], v2 offset0:36 offset1:38
	v_or_b32_e32 v150, s20, v231
	v_ashrrev_i32_e32 v151, 31, v150
	v_lshl_add_u64 v[148:149], v[216:217], 0, s[42:43]
	s_waitcnt lgkmcnt(1)
	v_mfma_f32_32x32x16_bf16 v[36:51], v[164:167], v[132:135], v[36:51]
	ds_read2_b64 v[132:135], v2 offset0:40 offset1:42
	s_waitcnt lgkmcnt(1)
	v_mfma_f32_32x32x16_bf16 v[36:51], v[168:171], v[136:139], v[36:51]
	s_waitcnt lgkmcnt(0)
	v_mfma_f32_32x32x16_bf16 v[36:51], v[176:179], v[132:135], v[36:51]
	ds_read2_b64 v[132:135], v2 offset0:44 offset1:46
	s_waitcnt lgkmcnt(0)
	v_mfma_f32_32x32x16_bf16 v[36:51], v[172:175], v[132:135], v[36:51]
	ds_read2_b64 v[132:135], v2 offset0:48 offset1:50
	ds_read2_b64 v[136:139], v2 offset0:52 offset1:54
	s_waitcnt lgkmcnt(1)
	v_mfma_f32_32x32x16_bf16 v[36:51], v[180:183], v[132:135], v[36:51]
	ds_read2_b64 v[132:135], v2 offset0:56 offset1:58
	s_waitcnt lgkmcnt(1)
	v_mfma_f32_32x32x16_bf16 v[36:51], v[184:187], v[136:139], v[36:51]
	s_waitcnt lgkmcnt(0)
	v_mfma_f32_32x32x16_bf16 v[36:51], v[192:195], v[132:135], v[36:51]
	ds_read2_b64 v[132:135], v2 offset0:60 offset1:62
	s_waitcnt lgkmcnt(0)
	v_mfma_f32_32x32x16_bf16 v[36:51], v[188:191], v[132:135], v[36:51]
	ds_read_b128 v[132:135], v140
	ds_read_b128 v[136:139], v140 offset:32
	ds_read_b128 v[160:163], v140 offset:64
	ds_read_b128 v[164:167], v140 offset:96
	s_waitcnt lgkmcnt(0)
	s_barrier
; __device__ __forceinline__ int crow(int r, int hi) { return (r & 3) + 8 * (r >> 2) + 4 * hi; }
; __device__ __forceinline__ int crow(int r,int hi){return (r&3)+8*(r>>2)+4*hi;}
; __device__ __forceinline__ void xattn_unit(Frame& F, const bf16* XQ, unsigned char* XO  , const bf16* MEMK, const bf16* MEMVT, int pm, int h) {
;     ...
;     float rl[16];
; #pragma unroll
;     for (int r = 0; r < 16; ++r) rl[r] = 1.0f / wsf[crow(r, hi)];
	v_div_scale_f32 v184, s[4:5], v132, v132, 1.0
	v_rcp_f32_e32 v185, v184
	s_nop 0
	v_fma_f32 v186, -v184, v185, 1.0
	v_fmac_f32_e32 v185, v186, v185
	v_div_scale_f32 v186, vcc, 1.0, v132, 1.0
	v_mul_f32_e32 v187, v186, v185
	v_fma_f32 v188, -v184, v187, v186
	v_fmac_f32_e32 v187, v188, v185
	v_fma_f32 v184, -v184, v187, v186
	v_div_fmas_f32 v184, v184, v185, v187
	v_div_fixup_f32 v168, v184, v132, 1.0
	v_div_scale_f32 v184, s[4:5], v133, v133, 1.0
	v_rcp_f32_e32 v185, v184
	s_nop 0
	v_fma_f32 v186, -v184, v185, 1.0
	v_fmac_f32_e32 v185, v186, v185
	v_div_scale_f32 v186, vcc, 1.0, v133, 1.0
	v_mul_f32_e32 v187, v186, v185
	v_fma_f32 v188, -v184, v187, v186
	v_fmac_f32_e32 v187, v188, v185
	v_fma_f32 v184, -v184, v187, v186
	v_div_fmas_f32 v184, v184, v185, v187
	v_div_fixup_f32 v169, v184, v133, 1.0
	v_div_scale_f32 v184, s[4:5], v134, v134, 1.0
	v_rcp_f32_e32 v185, v184
	s_nop 0
	v_fma_f32 v186, -v184, v185, 1.0
	v_fmac_f32_e32 v185, v186, v185
	v_div_scale_f32 v186, vcc, 1.0, v134, 1.0
	v_mul_f32_e32 v187, v186, v185
	v_fma_f32 v188, -v184, v187, v186
	v_fmac_f32_e32 v187, v188, v185
	v_fma_f32 v184, -v184, v187, v186
	v_div_fmas_f32 v184, v184, v185, v187
	v_div_fixup_f32 v170, v184, v134, 1.0
	v_div_scale_f32 v184, s[4:5], v135, v135, 1.0
	v_rcp_f32_e32 v185, v184
	s_nop 0
	v_fma_f32 v186, -v184, v185, 1.0
	v_fmac_f32_e32 v185, v186, v185
	v_div_scale_f32 v186, vcc, 1.0, v135, 1.0
	v_mul_f32_e32 v187, v186, v185
	v_fma_f32 v188, -v184, v187, v186
	v_fmac_f32_e32 v187, v188, v185
	v_fma_f32 v184, -v184, v187, v186
	v_div_fmas_f32 v184, v184, v185, v187
	v_div_fixup_f32 v171, v184, v135, 1.0
	v_div_scale_f32 v184, s[4:5], v136, v136, 1.0
	v_rcp_f32_e32 v185, v184
	s_nop 0
	v_fma_f32 v186, -v184, v185, 1.0
	v_fmac_f32_e32 v185, v186, v185
	v_div_scale_f32 v186, vcc, 1.0, v136, 1.0
	v_mul_f32_e32 v187, v186, v185
	v_fma_f32 v188, -v184, v187, v186
	v_fmac_f32_e32 v187, v188, v185
	v_fma_f32 v184, -v184, v187, v186
	v_div_fmas_f32 v184, v184, v185, v187
	v_div_fixup_f32 v172, v184, v136, 1.0
	v_div_scale_f32 v184, s[4:5], v137, v137, 1.0
	v_rcp_f32_e32 v185, v184
	s_nop 0
	v_fma_f32 v186, -v184, v185, 1.0
	v_fmac_f32_e32 v185, v186, v185
	v_div_scale_f32 v186, vcc, 1.0, v137, 1.0
	v_mul_f32_e32 v187, v186, v185
	v_fma_f32 v188, -v184, v187, v186
	v_fmac_f32_e32 v187, v188, v185
	v_fma_f32 v184, -v184, v187, v186
	v_div_fmas_f32 v184, v184, v185, v187
	v_div_fixup_f32 v173, v184, v137, 1.0
	v_div_scale_f32 v184, s[4:5], v138, v138, 1.0
	v_rcp_f32_e32 v185, v184
	s_nop 0
	v_fma_f32 v186, -v184, v185, 1.0
	v_fmac_f32_e32 v185, v186, v185
	v_div_scale_f32 v186, vcc, 1.0, v138, 1.0
	v_mul_f32_e32 v187, v186, v185
	v_fma_f32 v188, -v184, v187, v186
	v_fmac_f32_e32 v187, v188, v185
	v_fma_f32 v184, -v184, v187, v186
	v_div_fmas_f32 v184, v184, v185, v187
	v_div_fixup_f32 v174, v184, v138, 1.0
	v_div_scale_f32 v184, s[4:5], v139, v139, 1.0
	v_rcp_f32_e32 v185, v184
	s_nop 0
	v_fma_f32 v186, -v184, v185, 1.0
	v_fmac_f32_e32 v185, v186, v185
	v_div_scale_f32 v186, vcc, 1.0, v139, 1.0
	v_mul_f32_e32 v187, v186, v185
	v_fma_f32 v188, -v184, v187, v186
	v_fmac_f32_e32 v187, v188, v185
	v_fma_f32 v184, -v184, v187, v186
	v_div_fmas_f32 v184, v184, v185, v187
	v_div_fixup_f32 v175, v184, v139, 1.0
	v_div_scale_f32 v184, s[4:5], v160, v160, 1.0
	v_rcp_f32_e32 v185, v184
	s_nop 0
	v_fma_f32 v186, -v184, v185, 1.0
	v_fmac_f32_e32 v185, v186, v185
	v_div_scale_f32 v186, vcc, 1.0, v160, 1.0
	v_mul_f32_e32 v187, v186, v185
	v_fma_f32 v188, -v184, v187, v186
	v_fmac_f32_e32 v187, v188, v185
	v_fma_f32 v184, -v184, v187, v186
	v_div_fmas_f32 v184, v184, v185, v187
	v_div_fixup_f32 v176, v184, v160, 1.0
	v_div_scale_f32 v184, s[4:5], v161, v161, 1.0
	v_rcp_f32_e32 v185, v184
	s_nop 0
	v_fma_f32 v186, -v184, v185, 1.0
	v_fmac_f32_e32 v185, v186, v185
	v_div_scale_f32 v186, vcc, 1.0, v161, 1.0
	v_mul_f32_e32 v187, v186, v185
	v_fma_f32 v188, -v184, v187, v186
	v_fmac_f32_e32 v187, v188, v185
	v_fma_f32 v184, -v184, v187, v186
	v_div_fmas_f32 v184, v184, v185, v187
	v_div_fixup_f32 v177, v184, v161, 1.0
	v_div_scale_f32 v184, s[4:5], v162, v162, 1.0
	v_rcp_f32_e32 v185, v184
	s_nop 0
	v_fma_f32 v186, -v184, v185, 1.0
	v_fmac_f32_e32 v185, v186, v185
	v_div_scale_f32 v186, vcc, 1.0, v162, 1.0
	v_mul_f32_e32 v187, v186, v185
	v_fma_f32 v188, -v184, v187, v186
	v_fmac_f32_e32 v187, v188, v185
	v_fma_f32 v184, -v184, v187, v186
	v_div_fmas_f32 v184, v184, v185, v187
	v_div_fixup_f32 v178, v184, v162, 1.0
	v_div_scale_f32 v184, s[4:5], v163, v163, 1.0
	v_rcp_f32_e32 v185, v184
	s_nop 0
	v_fma_f32 v186, -v184, v185, 1.0
	v_fmac_f32_e32 v185, v186, v185
	v_div_scale_f32 v186, vcc, 1.0, v163, 1.0
	v_mul_f32_e32 v187, v186, v185
	v_fma_f32 v188, -v184, v187, v186
	v_fmac_f32_e32 v187, v188, v185
	v_fma_f32 v184, -v184, v187, v186
	v_div_fmas_f32 v184, v184, v185, v187
	v_div_fixup_f32 v179, v184, v163, 1.0
	v_div_scale_f32 v184, s[4:5], v164, v164, 1.0
	v_rcp_f32_e32 v185, v184
	s_nop 0
	v_fma_f32 v186, -v184, v185, 1.0
	v_fmac_f32_e32 v185, v186, v185
	v_div_scale_f32 v186, vcc, 1.0, v164, 1.0
	v_mul_f32_e32 v187, v186, v185
	v_fma_f32 v188, -v184, v187, v186
	v_fmac_f32_e32 v187, v188, v185
	v_fma_f32 v184, -v184, v187, v186
	v_div_fmas_f32 v184, v184, v185, v187
	v_div_fixup_f32 v180, v184, v164, 1.0
	v_div_scale_f32 v184, s[4:5], v165, v165, 1.0
	v_rcp_f32_e32 v185, v184
	s_nop 0
	v_fma_f32 v186, -v184, v185, 1.0
	v_fmac_f32_e32 v185, v186, v185
	v_div_scale_f32 v186, vcc, 1.0, v165, 1.0
	v_mul_f32_e32 v187, v186, v185
	v_fma_f32 v188, -v184, v187, v186
	v_fmac_f32_e32 v187, v188, v185
	v_fma_f32 v184, -v184, v187, v186
	v_div_fmas_f32 v184, v184, v185, v187
; __device__ __forceinline__ int crow(int r, int hi) { return (r & 3) + 8 * (r >> 2) + 4 * hi; }
; __device__ __forceinline__ int crow(int r,int hi){return (r&3)+8*(r>>2)+4*hi;}
; __device__ __forceinline__ void xattn_unit(Frame& F, const bf16* XQ, unsigned char* XO  , const bf16* MEMK, const bf16* MEMVT, int pm, int h) {
;     ...
;     float rl[16];
; #pragma unroll
;     for (int r = 0; r < 16; ++r) rl[r] = 1.0f / wsf[crow(r, hi)];
; #pragma unroll
;     for (int db = 0; db < 8; ++db)
; #pragma unroll
;         for (int r = 0; r < 16; ++r) XO[(size_t)(R0 + crow(r, hi)) * 1024 + h * 256 + db * 32 + r32] = (unsigned char)__builtin_amdgcn_cvt_pk_fp8_f32(o[db][r] * rl[r], 0.f, 0u, false);
	v_div_fixup_f32 v181, v184, v165, 1.0
	v_div_scale_f32 v184, s[4:5], v166, v166, 1.0
	v_rcp_f32_e32 v185, v184
	s_nop 0
	v_fma_f32 v186, -v184, v185, 1.0
	v_fmac_f32_e32 v185, v186, v185
	v_div_scale_f32 v186, vcc, 1.0, v166, 1.0
	v_mul_f32_e32 v187, v186, v185
	v_fma_f32 v188, -v184, v187, v186
	v_fmac_f32_e32 v187, v188, v185
	v_fma_f32 v184, -v184, v187, v186
	v_div_fmas_f32 v184, v184, v185, v187
	v_div_fixup_f32 v182, v184, v166, 1.0
	v_div_scale_f32 v184, s[4:5], v167, v167, 1.0
	v_rcp_f32_e32 v185, v184
	s_nop 0
	v_fma_f32 v186, -v184, v185, 1.0
	v_fmac_f32_e32 v185, v186, v185
	v_div_scale_f32 v186, vcc, 1.0, v167, 1.0
	v_mul_f32_e32 v187, v186, v185
	v_fma_f32 v188, -v184, v187, v186
	v_fmac_f32_e32 v187, v188, v185
	v_fma_f32 v184, -v184, v187, v186
	v_div_fmas_f32 v184, v184, v185, v187
	v_div_fixup_f32 v183, v184, v167, 1.0
	s_sub_i32 s58, s18, 0x21000
	s_mul_i32 s58, s58, 34
	s_movk_i32 s57, 0x110
	v_mad_u32_u24 v189, v231, s57, v212
	v_add_u32_e32 v189, s58, v189
	v_mul_f32_e32 v184, v116, v168
	v_cvt_pk_fp8_f32 v185, v184, 0
	ds_write_b8 v189, v185
	v_mul_f32_e32 v184, v117, v169
	v_cvt_pk_fp8_f32 v185, v184, 0
	ds_write_b8 v189, v185 offset:272
	v_mul_f32_e32 v184, v118, v170
	v_cvt_pk_fp8_f32 v185, v184, 0
	ds_write_b8 v189, v185 offset:544
	v_mul_f32_e32 v184, v119, v171
	v_cvt_pk_fp8_f32 v185, v184, 0
	ds_write_b8 v189, v185 offset:816
	v_mul_f32_e32 v184, v120, v172
	v_cvt_pk_fp8_f32 v185, v184, 0
	ds_write_b8 v189, v185 offset:2176
	v_mul_f32_e32 v184, v121, v173
	v_cvt_pk_fp8_f32 v185, v184, 0
	ds_write_b8 v189, v185 offset:2448
	v_mul_f32_e32 v184, v122, v174
	v_cvt_pk_fp8_f32 v185, v184, 0
	ds_write_b8 v189, v185 offset:2720
	v_mul_f32_e32 v184, v123, v175
	v_cvt_pk_fp8_f32 v185, v184, 0
	ds_write_b8 v189, v185 offset:2992
	v_mul_f32_e32 v184, v124, v176
	v_cvt_pk_fp8_f32 v185, v184, 0
	ds_write_b8 v189, v185 offset:4352
	v_mul_f32_e32 v184, v125, v177
	v_cvt_pk_fp8_f32 v185, v184, 0
	ds_write_b8 v189, v185 offset:4624
	v_mul_f32_e32 v184, v126, v178
	v_cvt_pk_fp8_f32 v185, v184, 0
	ds_write_b8 v189, v185 offset:4896
	v_mul_f32_e32 v184, v127, v179
	v_cvt_pk_fp8_f32 v185, v184, 0
	ds_write_b8 v189, v185 offset:5168
	v_mul_f32_e32 v184, v128, v180
	v_cvt_pk_fp8_f32 v185, v184, 0
	ds_write_b8 v189, v185 offset:6528
	v_mul_f32_e32 v184, v129, v181
	v_cvt_pk_fp8_f32 v185, v184, 0
	ds_write_b8 v189, v185 offset:6800
	v_mul_f32_e32 v184, v130, v182
	v_cvt_pk_fp8_f32 v185, v184, 0
	ds_write_b8 v189, v185 offset:7072
	v_mul_f32_e32 v184, v131, v183
	v_cvt_pk_fp8_f32 v185, v184, 0
	ds_write_b8 v189, v185 offset:7344
	v_mul_f32_e32 v184, v100, v168
	v_cvt_pk_fp8_f32 v185, v184, 0
	ds_write_b8 v189, v185 offset:32
	v_mul_f32_e32 v184, v101, v169
	v_cvt_pk_fp8_f32 v185, v184, 0
	ds_write_b8 v189, v185 offset:304
	v_mul_f32_e32 v184, v102, v170
	v_cvt_pk_fp8_f32 v185, v184, 0
	ds_write_b8 v189, v185 offset:576
	v_mul_f32_e32 v184, v103, v171
	v_cvt_pk_fp8_f32 v185, v184, 0
	ds_write_b8 v189, v185 offset:848
	v_mul_f32_e32 v184, v104, v172
	v_cvt_pk_fp8_f32 v185, v184, 0
	ds_write_b8 v189, v185 offset:2208
	v_mul_f32_e32 v184, v105, v173
	v_cvt_pk_fp8_f32 v185, v184, 0
	ds_write_b8 v189, v185 offset:2480
	v_mul_f32_e32 v184, v106, v174
	v_cvt_pk_fp8_f32 v185, v184, 0
	ds_write_b8 v189, v185 offset:2752
	v_mul_f32_e32 v184, v107, v175
	v_cvt_pk_fp8_f32 v185, v184, 0
	ds_write_b8 v189, v185 offset:3024
	v_mul_f32_e32 v184, v108, v176
	v_cvt_pk_fp8_f32 v185, v184, 0
	ds_write_b8 v189, v185 offset:4384
	v_mul_f32_e32 v184, v109, v177
	v_cvt_pk_fp8_f32 v185, v184, 0
	ds_write_b8 v189, v185 offset:4656
	v_mul_f32_e32 v184, v110, v178
	v_cvt_pk_fp8_f32 v185, v184, 0
	ds_write_b8 v189, v185 offset:4928
	v_mul_f32_e32 v184, v111, v179
	v_cvt_pk_fp8_f32 v185, v184, 0
	ds_write_b8 v189, v185 offset:5200
	v_mul_f32_e32 v184, v112, v180
	v_cvt_pk_fp8_f32 v185, v184, 0
	ds_write_b8 v189, v185 offset:6560
	v_mul_f32_e32 v184, v113, v181
	v_cvt_pk_fp8_f32 v185, v184, 0
	ds_write_b8 v189, v185 offset:6832
	v_mul_f32_e32 v184, v114, v182
	v_cvt_pk_fp8_f32 v185, v184, 0
	ds_write_b8 v189, v185 offset:7104
	v_mul_f32_e32 v184, v115, v183
	v_cvt_pk_fp8_f32 v185, v184, 0
	ds_write_b8 v189, v185 offset:7376
	v_mul_f32_e32 v184, v84, v168
	v_cvt_pk_fp8_f32 v185, v184, 0
	ds_write_b8 v189, v185 offset:64
	v_mul_f32_e32 v184, v85, v169
	v_cvt_pk_fp8_f32 v185, v184, 0
	ds_write_b8 v189, v185 offset:336
	v_mul_f32_e32 v184, v86, v170
	v_cvt_pk_fp8_f32 v185, v184, 0
	ds_write_b8 v189, v185 offset:608
	v_mul_f32_e32 v184, v87, v171
	v_cvt_pk_fp8_f32 v185, v184, 0
	ds_write_b8 v189, v185 offset:880
	v_mul_f32_e32 v184, v88, v172
	v_cvt_pk_fp8_f32 v185, v184, 0
	ds_write_b8 v189, v185 offset:2240
	v_mul_f32_e32 v184, v89, v173
	v_cvt_pk_fp8_f32 v185, v184, 0
	ds_write_b8 v189, v185 offset:2512
	v_mul_f32_e32 v184, v90, v174
	v_cvt_pk_fp8_f32 v185, v184, 0
	ds_write_b8 v189, v185 offset:2784
	v_mul_f32_e32 v184, v91, v175
	v_cvt_pk_fp8_f32 v185, v184, 0
	ds_write_b8 v189, v185 offset:3056
	v_mul_f32_e32 v184, v92, v176
	v_cvt_pk_fp8_f32 v185, v184, 0
	ds_write_b8 v189, v185 offset:4416
	v_mul_f32_e32 v184, v93, v177
	v_cvt_pk_fp8_f32 v185, v184, 0
	ds_write_b8 v189, v185 offset:4688
	v_mul_f32_e32 v184, v94, v178
	v_cvt_pk_fp8_f32 v185, v184, 0
	ds_write_b8 v189, v185 offset:4960
	v_mul_f32_e32 v184, v95, v179
	v_cvt_pk_fp8_f32 v185, v184, 0
	ds_write_b8 v189, v185 offset:5232
	v_mul_f32_e32 v184, v96, v180
	v_cvt_pk_fp8_f32 v185, v184, 0
	ds_write_b8 v189, v185 offset:6592
	v_mul_f32_e32 v184, v97, v181
	v_cvt_pk_fp8_f32 v185, v184, 0
	ds_write_b8 v189, v185 offset:6864
	v_mul_f32_e32 v184, v98, v182
	v_cvt_pk_fp8_f32 v185, v184, 0
	ds_write_b8 v189, v185 offset:7136
; __device__ __forceinline__ int crow(int r, int hi) { return (r & 3) + 8 * (r >> 2) + 4 * hi; }
; __device__ __forceinline__ int crow(int r,int hi){return (r&3)+8*(r>>2)+4*hi;}
; __device__ __forceinline__ void xattn_unit(Frame& F, const bf16* XQ, unsigned char* XO  , const bf16* MEMK, const bf16* MEMVT, int pm, int h) {
;     ...
; #pragma unroll
;     for (int db = 0; db < 8; ++db)
; #pragma unroll
;         for (int r = 0; r < 16; ++r) XO[(size_t)(R0 + crow(r, hi)) * 1024 + h * 256 + db * 32 + r32] = (unsigned char)__builtin_amdgcn_cvt_pk_fp8_f32(o[db][r] * rl[r], 0.f, 0u, false);
	v_mul_f32_e32 v184, v99, v183
	v_cvt_pk_fp8_f32 v185, v184, 0
	ds_write_b8 v189, v185 offset:7408
	v_mul_f32_e32 v184, v68, v168
	v_cvt_pk_fp8_f32 v185, v184, 0
	ds_write_b8 v189, v185 offset:96
	v_mul_f32_e32 v184, v69, v169
	v_cvt_pk_fp8_f32 v185, v184, 0
	ds_write_b8 v189, v185 offset:368
	v_mul_f32_e32 v184, v70, v170
	v_cvt_pk_fp8_f32 v185, v184, 0
	ds_write_b8 v189, v185 offset:640
	v_mul_f32_e32 v184, v71, v171
	v_cvt_pk_fp8_f32 v185, v184, 0
	ds_write_b8 v189, v185 offset:912
	v_mul_f32_e32 v184, v72, v172
	v_cvt_pk_fp8_f32 v185, v184, 0
	ds_write_b8 v189, v185 offset:2272
	v_mul_f32_e32 v184, v73, v173
	v_cvt_pk_fp8_f32 v185, v184, 0
	ds_write_b8 v189, v185 offset:2544
	v_mul_f32_e32 v184, v74, v174
	v_cvt_pk_fp8_f32 v185, v184, 0
	ds_write_b8 v189, v185 offset:2816
	v_mul_f32_e32 v184, v75, v175
	v_cvt_pk_fp8_f32 v185, v184, 0
	ds_write_b8 v189, v185 offset:3088
	v_mul_f32_e32 v184, v76, v176
	v_cvt_pk_fp8_f32 v185, v184, 0
	ds_write_b8 v189, v185 offset:4448
	v_mul_f32_e32 v184, v77, v177
	v_cvt_pk_fp8_f32 v185, v184, 0
	ds_write_b8 v189, v185 offset:4720
	v_mul_f32_e32 v184, v78, v178
	v_cvt_pk_fp8_f32 v185, v184, 0
	ds_write_b8 v189, v185 offset:4992
	v_mul_f32_e32 v184, v79, v179
	v_cvt_pk_fp8_f32 v185, v184, 0
	ds_write_b8 v189, v185 offset:5264
	v_mul_f32_e32 v184, v80, v180
	v_cvt_pk_fp8_f32 v185, v184, 0
	ds_write_b8 v189, v185 offset:6624
	v_mul_f32_e32 v184, v81, v181
	v_cvt_pk_fp8_f32 v185, v184, 0
	ds_write_b8 v189, v185 offset:6896
	v_mul_f32_e32 v184, v82, v182
	v_cvt_pk_fp8_f32 v185, v184, 0
	ds_write_b8 v189, v185 offset:7168
	v_mul_f32_e32 v184, v83, v183
	v_cvt_pk_fp8_f32 v185, v184, 0
	ds_write_b8 v189, v185 offset:7440
	v_mul_f32_e32 v184, v52, v168
	v_cvt_pk_fp8_f32 v185, v184, 0
	ds_write_b8 v189, v185 offset:128
	v_mul_f32_e32 v184, v53, v169
	v_cvt_pk_fp8_f32 v185, v184, 0
	ds_write_b8 v189, v185 offset:400
	v_mul_f32_e32 v184, v54, v170
	v_cvt_pk_fp8_f32 v185, v184, 0
	ds_write_b8 v189, v185 offset:672
	v_mul_f32_e32 v184, v55, v171
	v_cvt_pk_fp8_f32 v185, v184, 0
	ds_write_b8 v189, v185 offset:944
	v_mul_f32_e32 v184, v56, v172
	v_cvt_pk_fp8_f32 v185, v184, 0
	ds_write_b8 v189, v185 offset:2304
	v_mul_f32_e32 v184, v57, v173
	v_cvt_pk_fp8_f32 v185, v184, 0
	ds_write_b8 v189, v185 offset:2576
	v_mul_f32_e32 v184, v58, v174
	v_cvt_pk_fp8_f32 v185, v184, 0
	ds_write_b8 v189, v185 offset:2848
	v_mul_f32_e32 v184, v59, v175
	v_cvt_pk_fp8_f32 v185, v184, 0
	ds_write_b8 v189, v185 offset:3120
	v_mul_f32_e32 v184, v60, v176
	v_cvt_pk_fp8_f32 v185, v184, 0
	ds_write_b8 v189, v185 offset:4480
	v_mul_f32_e32 v184, v61, v177
	v_cvt_pk_fp8_f32 v185, v184, 0
	ds_write_b8 v189, v185 offset:4752
	v_mul_f32_e32 v184, v62, v178
	v_cvt_pk_fp8_f32 v185, v184, 0
	ds_write_b8 v189, v185 offset:5024
	v_mul_f32_e32 v184, v63, v179
	v_cvt_pk_fp8_f32 v185, v184, 0
	ds_write_b8 v189, v185 offset:5296
	v_mul_f32_e32 v184, v64, v180
	v_cvt_pk_fp8_f32 v185, v184, 0
	ds_write_b8 v189, v185 offset:6656
	v_mul_f32_e32 v184, v65, v181
	v_cvt_pk_fp8_f32 v185, v184, 0
	ds_write_b8 v189, v185 offset:6928
	v_mul_f32_e32 v184, v66, v182
	v_cvt_pk_fp8_f32 v185, v184, 0
	ds_write_b8 v189, v185 offset:7200
	v_mul_f32_e32 v184, v67, v183
	v_cvt_pk_fp8_f32 v185, v184, 0
	ds_write_b8 v189, v185 offset:7472
	v_mul_f32_e32 v184, v4, v168
	v_cvt_pk_fp8_f32 v185, v184, 0
	ds_write_b8 v189, v185 offset:160
	v_mul_f32_e32 v184, v5, v169
	v_cvt_pk_fp8_f32 v185, v184, 0
	ds_write_b8 v189, v185 offset:432
	v_mul_f32_e32 v184, v6, v170
	v_cvt_pk_fp8_f32 v185, v184, 0
	ds_write_b8 v189, v185 offset:704
	v_mul_f32_e32 v184, v7, v171
	v_cvt_pk_fp8_f32 v185, v184, 0
	ds_write_b8 v189, v185 offset:976
	v_mul_f32_e32 v184, v8, v172
	v_cvt_pk_fp8_f32 v185, v184, 0
	ds_write_b8 v189, v185 offset:2336
	v_mul_f32_e32 v184, v9, v173
	v_cvt_pk_fp8_f32 v185, v184, 0
	ds_write_b8 v189, v185 offset:2608
	v_mul_f32_e32 v184, v10, v174
	v_cvt_pk_fp8_f32 v185, v184, 0
	ds_write_b8 v189, v185 offset:2880
	v_mul_f32_e32 v184, v11, v175
	v_cvt_pk_fp8_f32 v185, v184, 0
	ds_write_b8 v189, v185 offset:3152
	v_mul_f32_e32 v184, v12, v176
	v_cvt_pk_fp8_f32 v185, v184, 0
	ds_write_b8 v189, v185 offset:4512
	v_mul_f32_e32 v184, v13, v177
	v_cvt_pk_fp8_f32 v185, v184, 0
	ds_write_b8 v189, v185 offset:4784
	v_mul_f32_e32 v184, v14, v178
	v_cvt_pk_fp8_f32 v185, v184, 0
	ds_write_b8 v189, v185 offset:5056
	v_mul_f32_e32 v184, v15, v179
	v_cvt_pk_fp8_f32 v185, v184, 0
	ds_write_b8 v189, v185 offset:5328
	v_mul_f32_e32 v184, v16, v180
	v_cvt_pk_fp8_f32 v185, v184, 0
	ds_write_b8 v189, v185 offset:6688
	v_mul_f32_e32 v184, v17, v181
	v_cvt_pk_fp8_f32 v185, v184, 0
	ds_write_b8 v189, v185 offset:6960
	v_mul_f32_e32 v184, v18, v182
	v_cvt_pk_fp8_f32 v185, v184, 0
	ds_write_b8 v189, v185 offset:7232
	v_mul_f32_e32 v184, v19, v183
	v_cvt_pk_fp8_f32 v185, v184, 0
	ds_write_b8 v189, v185 offset:7504
	v_mul_f32_e32 v184, v20, v168
	v_cvt_pk_fp8_f32 v185, v184, 0
	ds_write_b8 v189, v185 offset:192
; __device__ __forceinline__ int crow(int r, int hi) { return (r & 3) + 8 * (r >> 2) + 4 * hi; }
; __device__ __forceinline__ int crow(int r,int hi){return (r&3)+8*(r>>2)+4*hi;}
; __device__ __forceinline__ void xattn_unit(Frame& F, const bf16* XQ, unsigned char* XO  , const bf16* MEMK, const bf16* MEMVT, int pm, int h) {
;     ...
; #pragma unroll
;     for (int db = 0; db < 8; ++db)
; #pragma unroll
;         for (int r = 0; r < 16; ++r) XO[(size_t)(R0 + crow(r, hi)) * 1024 + h * 256 + db * 32 + r32] = (unsigned char)__builtin_amdgcn_cvt_pk_fp8_f32(o[db][r] * rl[r], 0.f, 0u, false);
;     __syncthreads();
	v_mul_f32_e32 v184, v21, v169
	v_cvt_pk_fp8_f32 v185, v184, 0
	ds_write_b8 v189, v185 offset:464
	v_mul_f32_e32 v184, v22, v170
	v_cvt_pk_fp8_f32 v185, v184, 0
	ds_write_b8 v189, v185 offset:736
	v_mul_f32_e32 v184, v23, v171
	v_cvt_pk_fp8_f32 v185, v184, 0
	ds_write_b8 v189, v185 offset:1008
	v_mul_f32_e32 v184, v24, v172
	v_cvt_pk_fp8_f32 v185, v184, 0
	ds_write_b8 v189, v185 offset:2368
	v_mul_f32_e32 v184, v25, v173
	v_cvt_pk_fp8_f32 v185, v184, 0
	ds_write_b8 v189, v185 offset:2640
	v_mul_f32_e32 v184, v26, v174
	v_cvt_pk_fp8_f32 v185, v184, 0
	ds_write_b8 v189, v185 offset:2912
	v_mul_f32_e32 v184, v27, v175
	v_cvt_pk_fp8_f32 v185, v184, 0
	ds_write_b8 v189, v185 offset:3184
	v_mul_f32_e32 v184, v28, v176
	v_cvt_pk_fp8_f32 v185, v184, 0
	ds_write_b8 v189, v185 offset:4544
	v_mul_f32_e32 v184, v29, v177
	v_cvt_pk_fp8_f32 v185, v184, 0
	ds_write_b8 v189, v185 offset:4816
	v_mul_f32_e32 v184, v30, v178
	v_cvt_pk_fp8_f32 v185, v184, 0
	ds_write_b8 v189, v185 offset:5088
	v_mul_f32_e32 v184, v31, v179
	v_cvt_pk_fp8_f32 v185, v184, 0
	ds_write_b8 v189, v185 offset:5360
	v_mul_f32_e32 v184, v32, v180
	v_cvt_pk_fp8_f32 v185, v184, 0
	ds_write_b8 v189, v185 offset:6720
	v_mul_f32_e32 v184, v33, v181
	v_cvt_pk_fp8_f32 v185, v184, 0
	ds_write_b8 v189, v185 offset:6992
	v_mul_f32_e32 v184, v34, v182
	v_cvt_pk_fp8_f32 v185, v184, 0
	ds_write_b8 v189, v185 offset:7264
	v_mul_f32_e32 v184, v35, v183
	v_cvt_pk_fp8_f32 v185, v184, 0
	ds_write_b8 v189, v185 offset:7536
	v_mul_f32_e32 v184, v36, v168
	v_cvt_pk_fp8_f32 v185, v184, 0
	ds_write_b8 v189, v185 offset:224
	v_mul_f32_e32 v184, v37, v169
	v_cvt_pk_fp8_f32 v185, v184, 0
	ds_write_b8 v189, v185 offset:496
	v_mul_f32_e32 v184, v38, v170
	v_cvt_pk_fp8_f32 v185, v184, 0
	ds_write_b8 v189, v185 offset:768
	v_mul_f32_e32 v184, v39, v171
	v_cvt_pk_fp8_f32 v185, v184, 0
	ds_write_b8 v189, v185 offset:1040
	v_mul_f32_e32 v184, v40, v172
	v_cvt_pk_fp8_f32 v185, v184, 0
	ds_write_b8 v189, v185 offset:2400
	v_mul_f32_e32 v184, v41, v173
	v_cvt_pk_fp8_f32 v185, v184, 0
	ds_write_b8 v189, v185 offset:2672
	v_mul_f32_e32 v184, v42, v174
	v_cvt_pk_fp8_f32 v185, v184, 0
	ds_write_b8 v189, v185 offset:2944
	v_mul_f32_e32 v184, v43, v175
	v_cvt_pk_fp8_f32 v185, v184, 0
	ds_write_b8 v189, v185 offset:3216
	v_mul_f32_e32 v184, v44, v176
	v_cvt_pk_fp8_f32 v185, v184, 0
	ds_write_b8 v189, v185 offset:4576
	v_mul_f32_e32 v184, v45, v177
	v_cvt_pk_fp8_f32 v185, v184, 0
	ds_write_b8 v189, v185 offset:4848
	v_mul_f32_e32 v184, v46, v178
	v_cvt_pk_fp8_f32 v185, v184, 0
	ds_write_b8 v189, v185 offset:5120
	v_mul_f32_e32 v184, v47, v179
	v_cvt_pk_fp8_f32 v185, v184, 0
	ds_write_b8 v189, v185 offset:5392
	v_mul_f32_e32 v184, v48, v180
	v_cvt_pk_fp8_f32 v185, v184, 0
	ds_write_b8 v189, v185 offset:6752
	v_mul_f32_e32 v184, v49, v181
	v_cvt_pk_fp8_f32 v185, v184, 0
	ds_write_b8 v189, v185 offset:7024
	v_mul_f32_e32 v184, v50, v182
	v_cvt_pk_fp8_f32 v185, v184, 0
	ds_write_b8 v189, v185 offset:7296
	v_mul_f32_e32 v184, v51, v183
	v_cvt_pk_fp8_f32 v185, v184, 0
	ds_write_b8 v189, v185 offset:7568
	v_and_b32_e32 v191, 63, v1
	v_lshrrev_b32_e32 v190, 4, v191
	v_and_b32_e32 v191, 15, v191
	v_add_u32_e32 v194, s20, v190
	v_mov_b32_e32 v195, 0
	v_lshlrev_b64 v[194:195], 10, v[194:195]
	v_mad_u32_u24 v190, v190, s57, 0
	v_lshl_add_u32 v190, v191, 4, v190
	v_add_u32_e32 v190, s58, v190
	v_lshlrev_b32_e32 v192, 4, v191
	v_sub_u32_e32 v192, v192, v212
	v_ashrrev_i32_e32 v193, 31, v192
	v_lshl_add_u64 v[192:193], v[148:149], 0, v[192:193]
	v_lshl_add_u64 v[192:193], v[192:193], 0, v[194:195]
	s_mov_b64 s[60:61], 0x1000
	s_waitcnt lgkmcnt(0)
	ds_read_b128 v[132:135], v190
	ds_read_b128 v[136:139], v190 offset:1088
	ds_read_b128 v[140:143], v190 offset:2176
	ds_read_b128 v[144:147], v190 offset:3264
	ds_read_b128 v[152:155], v190 offset:4352
	ds_read_b128 v[156:159], v190 offset:5440
	ds_read_b128 v[160:163], v190 offset:6528
	ds_read_b128 v[164:167], v190 offset:7616
	s_waitcnt lgkmcnt(7)
	global_store_dwordx4 v[192:193], v[132:135], off
	v_lshl_add_u64 v[192:193], v[192:193], 0, s[60:61]
	s_waitcnt lgkmcnt(6)
	global_store_dwordx4 v[192:193], v[136:139], off
	v_lshl_add_u64 v[192:193], v[192:193], 0, s[60:61]
	s_waitcnt lgkmcnt(5)
	global_store_dwordx4 v[192:193], v[140:143], off
	v_lshl_add_u64 v[192:193], v[192:193], 0, s[60:61]
	s_waitcnt lgkmcnt(4)
	global_store_dwordx4 v[192:193], v[144:147], off
	v_lshl_add_u64 v[192:193], v[192:193], 0, s[60:61]
	s_waitcnt lgkmcnt(3)
	global_store_dwordx4 v[192:193], v[152:155], off
	v_lshl_add_u64 v[192:193], v[192:193], 0, s[60:61]
	s_waitcnt lgkmcnt(2)
	global_store_dwordx4 v[192:193], v[156:159], off
	v_lshl_add_u64 v[192:193], v[192:193], 0, s[60:61]
	s_waitcnt lgkmcnt(1)
	global_store_dwordx4 v[192:193], v[160:163], off
	v_lshl_add_u64 v[192:193], v[192:193], 0, s[60:61]
	s_waitcnt lgkmcnt(0)
	global_store_dwordx4 v[192:193], v[164:167], off
	s_waitcnt vmcnt(63) expcnt(7) lgkmcnt(15)
	s_barrier
